# rowlist phase: 16 histogram loads in flight per trip (counted waits) instead of 16 serialized round trips; gate-up L0 unit header: 4 row-table lookups batched
# speedup vs baseline: 1.0707x; 1.0057x over previous
; __global__ void __launch_bounds__(NTHR, 2) mk(Params p) {
;     ...
;                 const int q_ = tid_ & 63, cg_ = tid_ >> 6, cpg_ = (F.G + 7) >> 3;
;                 i32x4 tot4 = {0, 0, 0, 0}, base4 = {0, 0, 0, 0};
; #pragma unroll 16
;                 for (int j = 0; j < cpg_; ++j) { const int c = cg_ * cpg_ + j;
;                     if (c < F.G) { const i32x4 v = *(const i32x4*)(HIST + (size_t)c * 256 + 4 * q_); tot4 += v; if (c < (int)blockIdx.x) base4 += v; } }
.LBB0_2052:
	v_add_u32_e32 v13, s6, v12
	v_readlane_b32 s8, v253, 2
	s_add_i32 s9, s59, -1
	v_min_i32_e32 v100, s9, v13
	v_lshlrev_b32_e32 v100, 10, v100
	v_mov_b32_e32 v101, 0
	v_lshl_add_u64 v[100:101], v[14:15], 0, v[100:101]
	global_load_dwordx4 v[100:103], v[100:101], off
	v_add_u32_e32 v104, 1, v13
	v_min_i32_e32 v104, s9, v104
	v_lshlrev_b32_e32 v104, 10, v104
	v_mov_b32_e32 v105, 0
	v_lshl_add_u64 v[104:105], v[14:15], 0, v[104:105]
	global_load_dwordx4 v[104:107], v[104:105], off
	v_add_u32_e32 v108, 2, v13
	v_min_i32_e32 v108, s9, v108
	v_lshlrev_b32_e32 v108, 10, v108
	v_mov_b32_e32 v109, 0
	v_lshl_add_u64 v[108:109], v[14:15], 0, v[108:109]
	global_load_dwordx4 v[108:111], v[108:109], off
	v_add_u32_e32 v112, 3, v13
	v_min_i32_e32 v112, s9, v112
	v_lshlrev_b32_e32 v112, 10, v112
	v_mov_b32_e32 v113, 0
	v_lshl_add_u64 v[112:113], v[14:15], 0, v[112:113]
	global_load_dwordx4 v[112:115], v[112:113], off
	v_add_u32_e32 v116, 4, v13
	v_min_i32_e32 v116, s9, v116
	v_lshlrev_b32_e32 v116, 10, v116
	v_mov_b32_e32 v117, 0
	v_lshl_add_u64 v[116:117], v[14:15], 0, v[116:117]
	global_load_dwordx4 v[116:119], v[116:117], off
	v_add_u32_e32 v120, 5, v13
	v_min_i32_e32 v120, s9, v120
	v_lshlrev_b32_e32 v120, 10, v120
	v_mov_b32_e32 v121, 0
	v_lshl_add_u64 v[120:121], v[14:15], 0, v[120:121]
	global_load_dwordx4 v[120:123], v[120:121], off
	v_add_u32_e32 v124, 6, v13
	v_min_i32_e32 v124, s9, v124
	v_lshlrev_b32_e32 v124, 10, v124
	v_mov_b32_e32 v125, 0
	v_lshl_add_u64 v[124:125], v[14:15], 0, v[124:125]
	global_load_dwordx4 v[124:127], v[124:125], off
	v_add_u32_e32 v128, 7, v13
	v_min_i32_e32 v128, s9, v128
	v_lshlrev_b32_e32 v128, 10, v128
	v_mov_b32_e32 v129, 0
	v_lshl_add_u64 v[128:129], v[14:15], 0, v[128:129]
	global_load_dwordx4 v[128:131], v[128:129], off
	v_add_u32_e32 v132, 8, v13
	v_min_i32_e32 v132, s9, v132
	v_lshlrev_b32_e32 v132, 10, v132
	v_mov_b32_e32 v133, 0
	v_lshl_add_u64 v[132:133], v[14:15], 0, v[132:133]
	global_load_dwordx4 v[132:135], v[132:133], off
	v_add_u32_e32 v136, 9, v13
	v_min_i32_e32 v136, s9, v136
	v_lshlrev_b32_e32 v136, 10, v136
	v_mov_b32_e32 v137, 0
	v_lshl_add_u64 v[136:137], v[14:15], 0, v[136:137]
	global_load_dwordx4 v[136:139], v[136:137], off
	v_add_u32_e32 v140, 10, v13
	v_min_i32_e32 v140, s9, v140
	v_lshlrev_b32_e32 v140, 10, v140
	v_mov_b32_e32 v141, 0
	v_lshl_add_u64 v[140:141], v[14:15], 0, v[140:141]
	global_load_dwordx4 v[140:143], v[140:141], off
	v_add_u32_e32 v144, 11, v13
	v_min_i32_e32 v144, s9, v144
	v_lshlrev_b32_e32 v144, 10, v144
	v_mov_b32_e32 v145, 0
	v_lshl_add_u64 v[144:145], v[14:15], 0, v[144:145]
	global_load_dwordx4 v[144:147], v[144:145], off
	v_add_u32_e32 v148, 12, v13
	v_min_i32_e32 v148, s9, v148
	v_lshlrev_b32_e32 v148, 10, v148
	v_mov_b32_e32 v149, 0
	v_lshl_add_u64 v[148:149], v[14:15], 0, v[148:149]
	global_load_dwordx4 v[148:151], v[148:149], off
	v_add_u32_e32 v152, 13, v13
	v_min_i32_e32 v152, s9, v152
	v_lshlrev_b32_e32 v152, 10, v152
	v_mov_b32_e32 v153, 0
	v_lshl_add_u64 v[152:153], v[14:15], 0, v[152:153]
	global_load_dwordx4 v[152:155], v[152:153], off
	v_add_u32_e32 v156, 14, v13
	v_min_i32_e32 v156, s9, v156
	v_lshlrev_b32_e32 v156, 10, v156
	v_mov_b32_e32 v157, 0
	v_lshl_add_u64 v[156:157], v[14:15], 0, v[156:157]
	global_load_dwordx4 v[156:159], v[156:157], off
	v_add_u32_e32 v160, 15, v13
	v_min_i32_e32 v160, s9, v160
	v_lshlrev_b32_e32 v160, 10, v160
	v_mov_b32_e32 v161, 0
	v_lshl_add_u64 v[160:161], v[14:15], 0, v[160:161]
	global_load_dwordx4 v[160:163], v[160:161], off
	s_waitcnt vmcnt(15)
	v_add_u32_e32 v18, 0, v13
	v_cmp_gt_i32_e32 vcc, s59, v18
	s_nop 1
	v_cndmask_b32_e32 v22, 0, v100, vcc
	v_cndmask_b32_e32 v23, 0, v101, vcc
	v_cndmask_b32_e32 v24, 0, v102, vcc
	v_cndmask_b32_e32 v25, 0, v103, vcc
	v_cmp_gt_i32_e32 vcc, s8, v18
	v_add_u32_e32 v2, v22, v2
	v_add_u32_e32 v3, v23, v3
	v_add_u32_e32 v4, v24, v4
	v_add_u32_e32 v5, v25, v5
	v_cndmask_b32_e32 v22, 0, v100, vcc
	v_cndmask_b32_e32 v23, 0, v101, vcc
	v_cndmask_b32_e32 v24, 0, v102, vcc
	v_cndmask_b32_e32 v25, 0, v103, vcc
	v_add_u32_e32 v6, v22, v6
	v_add_u32_e32 v7, v23, v7
	v_add_u32_e32 v8, v24, v8
	v_add_u32_e32 v9, v25, v9
	s_waitcnt vmcnt(14)
	v_add_u32_e32 v18, 1, v13
	v_cmp_gt_i32_e32 vcc, s59, v18
	s_nop 1
	v_cndmask_b32_e32 v22, 0, v104, vcc
	v_cndmask_b32_e32 v23, 0, v105, vcc
	v_cndmask_b32_e32 v24, 0, v106, vcc
	v_cndmask_b32_e32 v25, 0, v107, vcc
	v_cmp_gt_i32_e32 vcc, s8, v18
	v_add_u32_e32 v2, v22, v2
	v_add_u32_e32 v3, v23, v3
	v_add_u32_e32 v4, v24, v4
	v_add_u32_e32 v5, v25, v5
	v_cndmask_b32_e32 v22, 0, v104, vcc
	v_cndmask_b32_e32 v23, 0, v105, vcc
	v_cndmask_b32_e32 v24, 0, v106, vcc
	v_cndmask_b32_e32 v25, 0, v107, vcc
	v_add_u32_e32 v6, v22, v6
	v_add_u32_e32 v7, v23, v7
	v_add_u32_e32 v8, v24, v8
	v_add_u32_e32 v9, v25, v9
	s_waitcnt vmcnt(13)
	v_add_u32_e32 v18, 2, v13
	v_cmp_gt_i32_e32 vcc, s59, v18
	s_nop 1
	v_cndmask_b32_e32 v22, 0, v108, vcc
	v_cndmask_b32_e32 v23, 0, v109, vcc
	v_cndmask_b32_e32 v24, 0, v110, vcc
	v_cndmask_b32_e32 v25, 0, v111, vcc
	v_cmp_gt_i32_e32 vcc, s8, v18
	v_add_u32_e32 v2, v22, v2
	v_add_u32_e32 v3, v23, v3
	v_add_u32_e32 v4, v24, v4
	v_add_u32_e32 v5, v25, v5
	v_cndmask_b32_e32 v22, 0, v108, vcc
	v_cndmask_b32_e32 v23, 0, v109, vcc
	v_cndmask_b32_e32 v24, 0, v110, vcc
	v_cndmask_b32_e32 v25, 0, v111, vcc
	v_add_u32_e32 v6, v22, v6
	v_add_u32_e32 v7, v23, v7
	v_add_u32_e32 v8, v24, v8
	v_add_u32_e32 v9, v25, v9
	s_waitcnt vmcnt(12)
; __global__ void __launch_bounds__(NTHR, 2) mk(Params p) {
;     ...
;                 const int q_ = tid_ & 63, cg_ = tid_ >> 6, cpg_ = (F.G + 7) >> 3;
;                 i32x4 tot4 = {0, 0, 0, 0}, base4 = {0, 0, 0, 0};
; #pragma unroll 16
;                 for (int j = 0; j < cpg_; ++j) { const int c = cg_ * cpg_ + j;
;                     if (c < F.G) { const i32x4 v = *(const i32x4*)(HIST + (size_t)c * 256 + 4 * q_); tot4 += v; if (c < (int)blockIdx.x) base4 += v; } }
	v_add_u32_e32 v18, 3, v13
	v_cmp_gt_i32_e32 vcc, s59, v18
	s_nop 1
	v_cndmask_b32_e32 v22, 0, v112, vcc
	v_cndmask_b32_e32 v23, 0, v113, vcc
	v_cndmask_b32_e32 v24, 0, v114, vcc
	v_cndmask_b32_e32 v25, 0, v115, vcc
	v_cmp_gt_i32_e32 vcc, s8, v18
	v_add_u32_e32 v2, v22, v2
	v_add_u32_e32 v3, v23, v3
	v_add_u32_e32 v4, v24, v4
	v_add_u32_e32 v5, v25, v5
	v_cndmask_b32_e32 v22, 0, v112, vcc
	v_cndmask_b32_e32 v23, 0, v113, vcc
	v_cndmask_b32_e32 v24, 0, v114, vcc
	v_cndmask_b32_e32 v25, 0, v115, vcc
	v_add_u32_e32 v6, v22, v6
	v_add_u32_e32 v7, v23, v7
	v_add_u32_e32 v8, v24, v8
	v_add_u32_e32 v9, v25, v9
	s_waitcnt vmcnt(11)
	v_add_u32_e32 v18, 4, v13
	v_cmp_gt_i32_e32 vcc, s59, v18
	s_nop 1
	v_cndmask_b32_e32 v22, 0, v116, vcc
	v_cndmask_b32_e32 v23, 0, v117, vcc
	v_cndmask_b32_e32 v24, 0, v118, vcc
	v_cndmask_b32_e32 v25, 0, v119, vcc
	v_cmp_gt_i32_e32 vcc, s8, v18
	v_add_u32_e32 v2, v22, v2
	v_add_u32_e32 v3, v23, v3
	v_add_u32_e32 v4, v24, v4
	v_add_u32_e32 v5, v25, v5
	v_cndmask_b32_e32 v22, 0, v116, vcc
	v_cndmask_b32_e32 v23, 0, v117, vcc
	v_cndmask_b32_e32 v24, 0, v118, vcc
	v_cndmask_b32_e32 v25, 0, v119, vcc
	v_add_u32_e32 v6, v22, v6
	v_add_u32_e32 v7, v23, v7
	v_add_u32_e32 v8, v24, v8
	v_add_u32_e32 v9, v25, v9
	s_waitcnt vmcnt(10)
	v_add_u32_e32 v18, 5, v13
	v_cmp_gt_i32_e32 vcc, s59, v18
	s_nop 1
	v_cndmask_b32_e32 v22, 0, v120, vcc
	v_cndmask_b32_e32 v23, 0, v121, vcc
	v_cndmask_b32_e32 v24, 0, v122, vcc
	v_cndmask_b32_e32 v25, 0, v123, vcc
	v_cmp_gt_i32_e32 vcc, s8, v18
	v_add_u32_e32 v2, v22, v2
	v_add_u32_e32 v3, v23, v3
	v_add_u32_e32 v4, v24, v4
	v_add_u32_e32 v5, v25, v5
	v_cndmask_b32_e32 v22, 0, v120, vcc
	v_cndmask_b32_e32 v23, 0, v121, vcc
	v_cndmask_b32_e32 v24, 0, v122, vcc
	v_cndmask_b32_e32 v25, 0, v123, vcc
	v_add_u32_e32 v6, v22, v6
	v_add_u32_e32 v7, v23, v7
	v_add_u32_e32 v8, v24, v8
	v_add_u32_e32 v9, v25, v9
	s_waitcnt vmcnt(9)
	v_add_u32_e32 v18, 6, v13
	v_cmp_gt_i32_e32 vcc, s59, v18
	s_nop 1
	v_cndmask_b32_e32 v22, 0, v124, vcc
	v_cndmask_b32_e32 v23, 0, v125, vcc
	v_cndmask_b32_e32 v24, 0, v126, vcc
	v_cndmask_b32_e32 v25, 0, v127, vcc
	v_cmp_gt_i32_e32 vcc, s8, v18
	v_add_u32_e32 v2, v22, v2
	v_add_u32_e32 v3, v23, v3
	v_add_u32_e32 v4, v24, v4
	v_add_u32_e32 v5, v25, v5
	v_cndmask_b32_e32 v22, 0, v124, vcc
	v_cndmask_b32_e32 v23, 0, v125, vcc
	v_cndmask_b32_e32 v24, 0, v126, vcc
	v_cndmask_b32_e32 v25, 0, v127, vcc
	v_add_u32_e32 v6, v22, v6
	v_add_u32_e32 v7, v23, v7
	v_add_u32_e32 v8, v24, v8
	v_add_u32_e32 v9, v25, v9
	s_waitcnt vmcnt(8)
	v_add_u32_e32 v18, 7, v13
	v_cmp_gt_i32_e32 vcc, s59, v18
	s_nop 1
	v_cndmask_b32_e32 v22, 0, v128, vcc
	v_cndmask_b32_e32 v23, 0, v129, vcc
	v_cndmask_b32_e32 v24, 0, v130, vcc
	v_cndmask_b32_e32 v25, 0, v131, vcc
	v_cmp_gt_i32_e32 vcc, s8, v18
	v_add_u32_e32 v2, v22, v2
	v_add_u32_e32 v3, v23, v3
	v_add_u32_e32 v4, v24, v4
	v_add_u32_e32 v5, v25, v5
	v_cndmask_b32_e32 v22, 0, v128, vcc
	v_cndmask_b32_e32 v23, 0, v129, vcc
	v_cndmask_b32_e32 v24, 0, v130, vcc
	v_cndmask_b32_e32 v25, 0, v131, vcc
	v_add_u32_e32 v6, v22, v6
	v_add_u32_e32 v7, v23, v7
	v_add_u32_e32 v8, v24, v8
	v_add_u32_e32 v9, v25, v9
	s_waitcnt vmcnt(7)
	v_add_u32_e32 v18, 8, v13
	v_cmp_gt_i32_e32 vcc, s59, v18
	s_nop 1
	v_cndmask_b32_e32 v22, 0, v132, vcc
	v_cndmask_b32_e32 v23, 0, v133, vcc
	v_cndmask_b32_e32 v24, 0, v134, vcc
	v_cndmask_b32_e32 v25, 0, v135, vcc
	v_cmp_gt_i32_e32 vcc, s8, v18
	v_add_u32_e32 v2, v22, v2
	v_add_u32_e32 v3, v23, v3
	v_add_u32_e32 v4, v24, v4
	v_add_u32_e32 v5, v25, v5
	v_cndmask_b32_e32 v22, 0, v132, vcc
	v_cndmask_b32_e32 v23, 0, v133, vcc
	v_cndmask_b32_e32 v24, 0, v134, vcc
	v_cndmask_b32_e32 v25, 0, v135, vcc
	v_add_u32_e32 v6, v22, v6
	v_add_u32_e32 v7, v23, v7
	v_add_u32_e32 v8, v24, v8
	v_add_u32_e32 v9, v25, v9
	s_waitcnt vmcnt(6)
	v_add_u32_e32 v18, 9, v13
	v_cmp_gt_i32_e32 vcc, s59, v18
	s_nop 1
	v_cndmask_b32_e32 v22, 0, v136, vcc
	v_cndmask_b32_e32 v23, 0, v137, vcc
	v_cndmask_b32_e32 v24, 0, v138, vcc
	v_cndmask_b32_e32 v25, 0, v139, vcc
	v_cmp_gt_i32_e32 vcc, s8, v18
	v_add_u32_e32 v2, v22, v2
	v_add_u32_e32 v3, v23, v3
	v_add_u32_e32 v4, v24, v4
	v_add_u32_e32 v5, v25, v5
	v_cndmask_b32_e32 v22, 0, v136, vcc
	v_cndmask_b32_e32 v23, 0, v137, vcc
	v_cndmask_b32_e32 v24, 0, v138, vcc
	v_cndmask_b32_e32 v25, 0, v139, vcc
	v_add_u32_e32 v6, v22, v6
	v_add_u32_e32 v7, v23, v7
	v_add_u32_e32 v8, v24, v8
	v_add_u32_e32 v9, v25, v9
	s_waitcnt vmcnt(5)
; __global__ void __launch_bounds__(NTHR, 2) mk(Params p) {
;     ...
;                 const int q_ = tid_ & 63, cg_ = tid_ >> 6, cpg_ = (F.G + 7) >> 3;
;                 i32x4 tot4 = {0, 0, 0, 0}, base4 = {0, 0, 0, 0};
; #pragma unroll 16
;                 for (int j = 0; j < cpg_; ++j) { const int c = cg_ * cpg_ + j;
;                     if (c < F.G) { const i32x4 v = *(const i32x4*)(HIST + (size_t)c * 256 + 4 * q_); tot4 += v; if (c < (int)blockIdx.x) base4 += v; } }
	v_add_u32_e32 v18, 10, v13
	v_cmp_gt_i32_e32 vcc, s59, v18
	s_nop 1
	v_cndmask_b32_e32 v22, 0, v140, vcc
	v_cndmask_b32_e32 v23, 0, v141, vcc
	v_cndmask_b32_e32 v24, 0, v142, vcc
	v_cndmask_b32_e32 v25, 0, v143, vcc
	v_cmp_gt_i32_e32 vcc, s8, v18
	v_add_u32_e32 v2, v22, v2
	v_add_u32_e32 v3, v23, v3
	v_add_u32_e32 v4, v24, v4
	v_add_u32_e32 v5, v25, v5
	v_cndmask_b32_e32 v22, 0, v140, vcc
	v_cndmask_b32_e32 v23, 0, v141, vcc
	v_cndmask_b32_e32 v24, 0, v142, vcc
	v_cndmask_b32_e32 v25, 0, v143, vcc
	v_add_u32_e32 v6, v22, v6
	v_add_u32_e32 v7, v23, v7
	v_add_u32_e32 v8, v24, v8
	v_add_u32_e32 v9, v25, v9
	s_waitcnt vmcnt(4)
	v_add_u32_e32 v18, 11, v13
	v_cmp_gt_i32_e32 vcc, s59, v18
	s_nop 1
	v_cndmask_b32_e32 v22, 0, v144, vcc
	v_cndmask_b32_e32 v23, 0, v145, vcc
	v_cndmask_b32_e32 v24, 0, v146, vcc
	v_cndmask_b32_e32 v25, 0, v147, vcc
	v_cmp_gt_i32_e32 vcc, s8, v18
	v_add_u32_e32 v2, v22, v2
	v_add_u32_e32 v3, v23, v3
	v_add_u32_e32 v4, v24, v4
	v_add_u32_e32 v5, v25, v5
	v_cndmask_b32_e32 v22, 0, v144, vcc
	v_cndmask_b32_e32 v23, 0, v145, vcc
	v_cndmask_b32_e32 v24, 0, v146, vcc
	v_cndmask_b32_e32 v25, 0, v147, vcc
	v_add_u32_e32 v6, v22, v6
	v_add_u32_e32 v7, v23, v7
	v_add_u32_e32 v8, v24, v8
	v_add_u32_e32 v9, v25, v9
	s_waitcnt vmcnt(3)
	v_add_u32_e32 v18, 12, v13
	v_cmp_gt_i32_e32 vcc, s59, v18
	s_nop 1
	v_cndmask_b32_e32 v22, 0, v148, vcc
	v_cndmask_b32_e32 v23, 0, v149, vcc
	v_cndmask_b32_e32 v24, 0, v150, vcc
	v_cndmask_b32_e32 v25, 0, v151, vcc
	v_cmp_gt_i32_e32 vcc, s8, v18
	v_add_u32_e32 v2, v22, v2
	v_add_u32_e32 v3, v23, v3
	v_add_u32_e32 v4, v24, v4
	v_add_u32_e32 v5, v25, v5
	v_cndmask_b32_e32 v22, 0, v148, vcc
	v_cndmask_b32_e32 v23, 0, v149, vcc
	v_cndmask_b32_e32 v24, 0, v150, vcc
	v_cndmask_b32_e32 v25, 0, v151, vcc
	v_add_u32_e32 v6, v22, v6
	v_add_u32_e32 v7, v23, v7
	v_add_u32_e32 v8, v24, v8
	v_add_u32_e32 v9, v25, v9
	s_waitcnt vmcnt(2)
	v_add_u32_e32 v18, 13, v13
	v_cmp_gt_i32_e32 vcc, s59, v18
	s_nop 1
	v_cndmask_b32_e32 v22, 0, v152, vcc
	v_cndmask_b32_e32 v23, 0, v153, vcc
	v_cndmask_b32_e32 v24, 0, v154, vcc
	v_cndmask_b32_e32 v25, 0, v155, vcc
	v_cmp_gt_i32_e32 vcc, s8, v18
	v_add_u32_e32 v2, v22, v2
	v_add_u32_e32 v3, v23, v3
	v_add_u32_e32 v4, v24, v4
	v_add_u32_e32 v5, v25, v5
	v_cndmask_b32_e32 v22, 0, v152, vcc
	v_cndmask_b32_e32 v23, 0, v153, vcc
	v_cndmask_b32_e32 v24, 0, v154, vcc
	v_cndmask_b32_e32 v25, 0, v155, vcc
	v_add_u32_e32 v6, v22, v6
	v_add_u32_e32 v7, v23, v7
	v_add_u32_e32 v8, v24, v8
	v_add_u32_e32 v9, v25, v9
	s_waitcnt vmcnt(1)
	v_add_u32_e32 v18, 14, v13
	v_cmp_gt_i32_e32 vcc, s59, v18
	s_nop 1
	v_cndmask_b32_e32 v22, 0, v156, vcc
	v_cndmask_b32_e32 v23, 0, v157, vcc
	v_cndmask_b32_e32 v24, 0, v158, vcc
	v_cndmask_b32_e32 v25, 0, v159, vcc
	v_cmp_gt_i32_e32 vcc, s8, v18
	v_add_u32_e32 v2, v22, v2
	v_add_u32_e32 v3, v23, v3
	v_add_u32_e32 v4, v24, v4
	v_add_u32_e32 v5, v25, v5
	v_cndmask_b32_e32 v22, 0, v156, vcc
	v_cndmask_b32_e32 v23, 0, v157, vcc
	v_cndmask_b32_e32 v24, 0, v158, vcc
	v_cndmask_b32_e32 v25, 0, v159, vcc
	v_add_u32_e32 v6, v22, v6
	v_add_u32_e32 v7, v23, v7
	v_add_u32_e32 v8, v24, v8
	v_add_u32_e32 v9, v25, v9
	s_waitcnt vmcnt(0)
	v_add_u32_e32 v18, 15, v13
	v_cmp_gt_i32_e32 vcc, s59, v18
	s_nop 1
	v_cndmask_b32_e32 v22, 0, v160, vcc
	v_cndmask_b32_e32 v23, 0, v161, vcc
	v_cndmask_b32_e32 v24, 0, v162, vcc
	v_cndmask_b32_e32 v25, 0, v163, vcc
	v_cmp_gt_i32_e32 vcc, s8, v18
	v_add_u32_e32 v2, v22, v2
	v_add_u32_e32 v3, v23, v3
	v_add_u32_e32 v4, v24, v4
	v_add_u32_e32 v5, v25, v5
	v_cndmask_b32_e32 v22, 0, v160, vcc
	v_cndmask_b32_e32 v23, 0, v161, vcc
	v_cndmask_b32_e32 v24, 0, v162, vcc
	v_cndmask_b32_e32 v25, 0, v163, vcc
	v_add_u32_e32 v6, v22, v6
	v_add_u32_e32 v7, v23, v7
	v_add_u32_e32 v8, v24, v8
	v_add_u32_e32 v9, v25, v9
	s_branch .LBB0_2051

.LBB0_2248:
	v_cndmask_b32_e64 v34, 0, 1, s[4:5]
	v_cmp_ne_u32_e64 s[0:1], 1, v34
	s_andn2_b64 vcc, exec, s[4:5]
	v_mov_b32_e32 v242, v226
	v_mov_b32_e32 v243, v228
	v_mov_b32_e32 v244, v234
	v_mov_b32_e32 v245, v235
	s_cbranch_vccnz .LBB0_2250
	v_mov_b32_e32 v34, v1
	s_add_i32 s2, s49, -1
	v_ashrrev_i32_e32 v36, 31, v34
	v_lshrrev_b32_e32 v36, 26, v36
	v_lshlrev_b32_e32 v35, 4, v34
	v_add_u32_e32 v36, v34, v36
	v_bfe_i32 v34, v34, 27, 1
	v_lshrrev_b32_e32 v34, 22, v34
	v_add_u32_e32 v34, v35, v34
	v_and_b32_e32 v34, 0xfffffc00, v34
	v_sub_u32_e32 v34, v35, v34
	v_lshrrev_b32_e32 v37, 4, v34
	v_bitop3_b32 v34, v37, v34, 32 bitop3:0x6c
	v_ashrrev_i32_e32 v38, 31, v34
	v_lshrrev_b32_e32 v38, 26, v38
	v_add_u32_e32 v38, v34, v38
	v_ashrrev_i32_e32 v39, 6, v38
	v_and_b32_e32 v38, 0xc0, v38
	v_ashrrev_i32_e32 v36, 6, v36
	v_sub_u32_e32 v34, v34, v38
	v_lshlrev_b32_e32 v37, 3, v36
	v_lshlrev_b32_e32 v36, 5, v36
	v_ashrrev_i16_sdwa v34, v233, sext(v34) dst_sel:DWORD dst_unused:UNUSED_PAD src0_sel:DWORD src1_sel:BYTE_0
	v_and_b32_e32 v36, 32, v36
	v_bfe_i32 v34, v34, 0, 16
	v_add_lshl_u32 v36, v36, v34, 1
	v_add_u32_e32 v34, 0x2000, v35
	v_ashrrev_i32_e32 v35, 31, v34
	v_lshrrev_b32_e32 v35, 22, v35
	v_add_u32_e32 v35, v34, v35
	v_ashrrev_i32_e32 v35, 10, v35
	v_mul_i32_i24_e32 v38, 0x400, v35
	v_sub_u32_e32 v34, v34, v38
	v_lshrrev_b32_e32 v38, 4, v34
	v_and_b32_e32 v37, -16, v37
	v_bitop3_b32 v34, v38, v34, 32 bitop3:0x6c
	v_add_u32_e32 v37, v39, v37
	v_ashrrev_i32_e32 v39, 31, v34
	v_lshrrev_b32_e32 v39, 26, v39
	v_add_u32_e32 v39, v34, v39
	v_ashrrev_i32_e32 v40, 6, v39
	v_and_b32_e32 v39, 0xc0, v39
	v_sub_u32_e32 v34, v34, v39
	v_lshlrev_b32_e32 v38, 3, v35
	v_lshlrev_b32_e32 v35, 5, v35
	v_ashrrev_i16_sdwa v34, v233, sext(v34) dst_sel:DWORD dst_unused:UNUSED_PAD src0_sel:DWORD src1_sel:BYTE_0
	v_and_b32_e32 v35, 32, v35
	v_bfe_i32 v34, v34, 0, 16
	v_add_lshl_u32 v39, v35, v34, 1
	v_readlane_b32 s16, v254, 47
	v_readlane_b32 s17, v254, 48
	v_and_b32_e32 v38, -16, v38
	v_add_u32_e32 v38, v40, v38
	s_add_i32 s6, s50, 0x80
	v_add_u32_e32 v34, s50, v37
	v_min_i32_e32 v34, s2, v34
	v_ashrrev_i32_e32 v35, 31, v34
	v_lshl_add_u64 v[34:35], v[34:35], 2, s[16:17]
	v_add_u32_e32 v40, s50, v38
	v_min_i32_e32 v40, s2, v40
	v_ashrrev_i32_e32 v41, 31, v40
	v_lshl_add_u64 v[40:41], v[40:41], 2, s[16:17]
	v_add_u32_e32 v42, s6, v37
	v_min_i32_e32 v42, s2, v42
	v_ashrrev_i32_e32 v43, 31, v42
	v_lshl_add_u64 v[42:43], v[42:43], 2, s[16:17]
	v_add_u32_e32 v44, s6, v38
	v_min_i32_e32 v44, s2, v44
	v_ashrrev_i32_e32 v45, 31, v44
	v_lshl_add_u64 v[44:45], v[44:45], 2, s[16:17]
	global_load_dword v34, v[34:35], off
	global_load_dword v40, v[40:41], off
	global_load_dword v42, v[42:43], off
	global_load_dword v44, v[44:45], off
	s_waitcnt vmcnt(0)
	v_lshlrev_b32_e32 v34, 8, v34
	v_lshlrev_b32_e32 v40, 8, v40
	v_lshlrev_b32_e32 v42, 8, v42
	v_lshlrev_b32_e32 v44, 8, v44
	v_and_b32_e32 v34, 0xfffff800, v34
	v_and_b32_e32 v40, 0xfffff800, v40
	v_and_b32_e32 v42, 0xfffff800, v42
	v_and_b32_e32 v44, 0xfffff800, v44
	v_add_u32_e32 v242, v36, v34
	v_add_u32_e32 v243, v39, v40
	v_add_u32_e32 v244, v36, v42
	v_add_u32_e32 v245, v39, v44
